# k_gemm: one static s_setprio 1 for waves 4-7 (later-dispatched half) before the main loop
# speedup vs baseline: 1.0022x; 1.0022x over previous
_Z6k_gemmPKfPKDv8_DF16_S0_S0_PDF16_:
	s_load_dwordx2 s[8:9], s[0:1], 0x0
	s_load_dwordx2 s[10:11], s[0:1], 0x10
	s_load_dwordx2 s[12:13], s[0:1], 0x8
	s_load_dwordx4 s[4:7], s[0:1], 0x18
	s_mul_i32 s14, s2, 0xc4
	v_lshrrev_b32_e32 v1, 5, v0
	v_and_b32_e32 v89, 31, v0
	v_add_u32_e32 v2, s14, v1
	v_lshlrev_b32_e32 v154, 4, v89
	s_movk_i32 s15, 0x1664
	v_mad_u64_u32 v[150:151], s[0:1], v2, s15, v[154:155]
	s_lshl_b32 s16, s2, 2
	v_mul_u32_u24_e32 v245, 25, v1
	v_add_u32_e32 v245, s16, v245
	v_and_b32_e32 v245, 31, v245
	v_xor_b32_e32 v246, 16, v245
	v_lshlrev_b32_e32 v247, 2, v246
	v_sub_u32_e32 v244, v150, v247
	v_lshlrev_b32_e32 v247, 2, v245
	v_sub_u32_e32 v150, v150, v247
	v_add_u32_e32 v247, 24, v245
	v_lshrrev_b32_e32 v247, 2, v247
	v_sub_u32_e32 v247, v89, v247
	v_max_i32_e32 v247, 0, v247
	v_lshlrev_b32_e32 v247, 4, v247
	v_sub_u32_e32 v250, v150, v247
	v_add_u32_e32 v247, 24, v246
	v_lshrrev_b32_e32 v247, 2, v247
	v_sub_u32_e32 v247, v89, v247
	v_max_i32_e32 v247, 0, v247
	v_lshlrev_b32_e32 v247, 4, v247
	v_sub_u32_e32 v251, v244, v247
	s_movk_i32 s17, 0x1ee0
	v_mul_u32_u24_e32 v242, s17, v1
	v_add_u32_e32 v243, 0xffffff00, v242
	v_lshl_add_u32 v247, v89, 3, v242
	v_lshlrev_b32_e32 v248, 1, v245
	v_sub_u32_e32 v248, v247, v248
	v_add_u32_e32 v234, 64, v248
	v_add_u32_e32 v235, 0x42, v248
	v_add_u32_e32 v236, 0x44, v248
	v_add_u32_e32 v237, 0x46, v248
	v_lshlrev_b32_e32 v248, 1, v246
	v_sub_u32_e32 v248, v247, v248
	v_add_u32_e32 v238, 64, v248
	v_add_u32_e32 v239, 0x42, v248
	v_add_u32_e32 v240, 0x44, v248
	v_add_u32_e32 v241, 0x46, v248
	v_and_b32_e32 v247, 7, v89
	v_lshl_add_u32 v247, v247, 3, v242
	v_mov_b32_e32 v248, 0
	v_mov_b32_e32 v249, 0
	ds_write_b64 v247, v[248:249] offset:0
	ds_write_b64 v247, v[248:249] offset:608
	ds_write_b64 v247, v[248:249] offset:1216
	ds_write_b64 v247, v[248:249] offset:1824
	ds_write_b64 v247, v[248:249] offset:2432
	ds_write_b64 v247, v[248:249] offset:3040
	ds_write_b64 v247, v[248:249] offset:3648
	ds_write_b64 v247, v[248:249] offset:4256
	ds_write_b64 v247, v[248:249] offset:4864
	ds_write_b64 v247, v[248:249] offset:5472
	ds_write_b64 v247, v[248:249] offset:6080
	ds_write_b64 v247, v[248:249] offset:6688
	ds_write_b64 v247, v[248:249] offset:7296
	v_lshrrev_b32_e32 v245, 8, v0
	s_nop 0
	v_readfirstlane_b32 s16, v245
	s_cmp_eq_u32 s16, 0
	s_cbranch_scc1 .Lgemm_noprio
	s_setprio 1
.Lgemm_noprio:
	v_mov_b32_e32 v2, 2
	v_lshlrev_b32_sdwa v2, v2, v0 dst_sel:DWORD dst_unused:UNUSED_PAD src0_sel:DWORD src1_sel:BYTE_0
	v_mov_b32_e32 v3, 0
	s_waitcnt lgkmcnt(0)
	v_lshl_add_u64 v[4:5], s[4:5], 0, v[2:3]
	s_mov_b32 s0, 0x166000
	v_add_co_u32_e32 v4, vcc, s0, v4
	v_add_u32_e32 v6, 0x111514dc, v154
	s_nop 0
	v_addc_co_u32_e32 v5, vcc, 0, v5, vcc
	global_load_dword v90, v[4:5], off
	v_add_u32_e32 v4, 0x16640, v244
	v_min_u32_e32 v2, v150, v6
	v_min_u32_e32 v4, v4, v6
	global_load_dwordx4 v[82:85], v2, s[8:9] nt
	global_load_dwordx4 v[78:81], v4, s[8:9] nt
	v_add_u32_e32 v2, 0x2cc80, v150
	v_min_u32_e32 v2, v2, v6
	v_add_u32_e32 v4, 0x432c0, v244
	v_min_u32_e32 v4, v4, v6
	global_load_dwordx4 v[74:77], v2, s[8:9] nt
	global_load_dwordx4 v[70:73], v4, s[8:9] nt
	v_add_u32_e32 v2, 0x59900, v150
	v_min_u32_e32 v2, v2, v6
	v_add_u32_e32 v4, 0x6ff40, v244
	v_min_u32_e32 v4, v4, v6
	global_load_dwordx4 v[66:69], v2, s[8:9] nt
	global_load_dwordx4 v[54:57], v4, s[8:9] nt
	v_add_u32_e32 v2, 0x86580, v150
	v_min_u32_e32 v2, v2, v6
	v_add_u32_e32 v4, 0x9cbc0, v244
	v_min_u32_e32 v4, v4, v6
	global_load_dwordx4 v[62:65], v2, s[8:9] nt
	global_load_dwordx4 v[58:61], v4, s[8:9] nt
	v_add_u32_e32 v2, 0xb3200, v150
	v_min_u32_e32 v2, v2, v6
	v_add_u32_e32 v4, 0xc9840, v244
	v_min_u32_e32 v4, v4, v6
	global_load_dwordx4 v[46:49], v2, s[8:9] nt
	global_load_dwordx4 v[38:41], v4, s[8:9] nt
	v_add_u32_e32 v2, 0xdfe80, v150
	v_min_u32_e32 v2, v2, v6
	v_add_u32_e32 v4, 0xf64c0, v244
	s_movk_i32 s3, 0xc4
	v_or_b32_e32 v7, 0xc0, v1
	v_min_u32_e32 v4, v4, v6
	global_load_dwordx4 v[34:37], v2, s[8:9] nt
	global_load_dwordx4 v[14:17], v4, s[8:9] nt
	v_add_u32_e32 v2, 0x10cb00, v150
	v_min_u32_e32 v2, v2, v6
	v_cmp_gt_u32_e64 s[0:1], s3, v7
	v_bfe_u32 v87, v0, 4, 2
	v_and_b32_e32 v86, 15, v0
	v_cndmask_b32_e64 v2, 0, v2, s[0:1]
	global_load_dwordx4 v[10:13], v2, s[8:9] nt
	v_lshlrev_b32_e32 v2, 12, v87
	v_lshl_add_u64 v[4:5], s[12:13], 0, v[2:3]
	v_lshlrev_b32_e32 v2, 3, v0
	v_and_b32_e32 v2, 0xe00, v2
	v_lshl_add_u64 v[4:5], v[4:5], 0, v[2:3]
	v_lshlrev_b32_e32 v2, 4, v86
	v_lshl_add_u64 v[152:153], v[4:5], 0, v[2:3]
	s_movk_i32 s2, 0x4000
	v_add_co_u32_e32 v2, vcc, s2, v152
	s_mov_b32 s2, 0x8000
	s_nop 0
	v_addc_co_u32_e32 v3, vcc, 0, v153, vcc
	global_load_dwordx4 v[26:29], v[152:153], off sc1
	global_load_dwordx4 v[50:53], v[152:153], off offset:256 sc1
	global_load_dwordx4 v[18:21], v[2:3], off sc1
	global_load_dwordx4 v[42:45], v[2:3], off offset:256 sc1
	v_add_co_u32_e32 v2, vcc, s2, v152
	s_movk_i32 s2, 0xd0
	s_nop 0
	v_addc_co_u32_e32 v3, vcc, 0, v153, vcc
	v_add_co_u32_e32 v92, vcc, 0xc000, v152
	global_load_dwordx4 v[22:25], v[2:3], off sc1
	global_load_dwordx4 v[30:33], v[2:3], off offset:256 sc1
	v_addc_co_u32_e32 v93, vcc, 0, v153, vcc
	global_load_dwordx4 v[6:9], v[92:93], off sc1
	global_load_dwordx4 v[2:5], v[92:93], off offset:256 sc1
	v_cmp_gt_u32_e32 vcc, s2, v0
	v_add_u32_e32 v88, 0x111516dc, v154
	s_and_saveexec_b64 s[4:5], vcc
	s_cbranch_execz .LBB2_5
	v_cndmask_b32_e32 v91, 0, v0, vcc
	v_cmp_gt_u32_e32 vcc, s3, v91
	v_add_u32_e32 v91, s14, v91
	s_mov_b32 s2, 0xc350
	v_cmp_gt_i32_e64 s[2:3], s2, v91
	v_ashrrev_i32_e32 v92, 31, v91
	s_and_b64 s[2:3], vcc, s[2:3]
	v_cndmask_b32_e64 v93, 0, v92, s[2:3]
	v_mov_b32_e32 v92, 0xc34f
	v_cndmask_b32_e64 v92, v92, v91, s[2:3]
	v_mov_b64_e32 v[94:95], s[8:9]
	v_mad_i64_i32 v[94:95], s[12:13], v92, s15, v[94:95]
	v_add_co_u32_e32 v94, vcc, 0x1000, v94
	v_lshl_add_u64 v[92:93], v[92:93], 2, s[10:11]
	s_nop 0
	v_addc_co_u32_e32 v95, vcc, 0, v95, vcc
	global_load_dword v252, v[92:93], off
	global_load_dword v253, v[94:95], off offset:1632
	s_mov_b64 s[18:19], s[2:3]
